# k_csr: degree-count pass without per-entry branches (all 32 run masks first, then predicated LDS adds)
# speedup vs baseline: 1.0066x; 1.0066x over previous
.LBB1_7:
	s_or_b64 exec, exec, s[6:7]
	s_load_dwordx2 s[84:85], s[0:1], 0x8
	v_mul_u32_u24_e32 v38, 0x30d4, v0
	v_mov_b32_e32 v39, 0
	v_ashrrev_i32_e32 v35, 31, v34
	s_waitcnt vmcnt(0)
	v_sub_u32_e32 v1, v1, v34
	s_waitcnt lgkmcnt(0)
	v_lshl_add_u64 v[2:3], s[84:85], 0, v[38:39]
	v_lshl_add_u64 v[44:45], v[34:35], 2, v[2:3]
	global_load_dwordx4 v[18:21], v[44:45], off offset:48
	global_load_dwordx4 v[22:25], v[44:45], off offset:32
	global_load_dwordx4 v[26:29], v[44:45], off offset:16
	global_load_dwordx4 v[30:33], v[44:45], off
	global_load_dwordx4 v[2:5], v[44:45], off offset:112
	global_load_dwordx4 v[6:9], v[44:45], off offset:96
	global_load_dwordx4 v[10:13], v[44:45], off offset:80
	global_load_dwordx4 v[14:17], v[44:45], off offset:64
	v_or_b32_e32 v43, 0x4000, v40
	v_mov_b32_e32 v44, 2
	v_mov_b32_e32 v45, 1
	s_mov_b64 s[0:1], exec
	v_cmp_lt_i32_e64 s[30:31], 0, v1
	v_cmp_lt_i32_e64 s[66:67], 1, v1
	v_cmp_lt_i32_e64 s[64:65], 2, v1
	v_cmp_lt_i32_e64 s[62:63], 3, v1
	v_cmp_lt_i32_e64 s[60:61], 4, v1
	v_cmp_lt_i32_e64 s[58:59], 5, v1
	v_cmp_lt_i32_e64 s[56:57], 6, v1
	v_cmp_lt_i32_e64 s[54:55], 7, v1
	v_cmp_lt_i32_e64 s[52:53], 8, v1
	v_cmp_lt_i32_e64 s[50:51], 9, v1
	v_cmp_lt_i32_e64 s[48:49], 10, v1
	v_cmp_lt_i32_e64 s[46:47], 11, v1
	v_cmp_lt_i32_e64 s[44:45], 12, v1
	v_cmp_lt_i32_e64 s[42:43], 13, v1
	v_cmp_lt_i32_e64 s[40:41], 14, v1
	v_cmp_lt_i32_e64 s[38:39], 15, v1
	v_cmp_lt_i32_e64 s[36:37], 16, v1
	v_cmp_lt_i32_e64 s[34:35], 17, v1
	v_cmp_lt_i32_e64 s[28:29], 18, v1
	v_cmp_lt_i32_e64 s[26:27], 19, v1
	v_cmp_lt_i32_e64 s[24:25], 20, v1
	v_cmp_lt_i32_e64 s[22:23], 21, v1
	v_cmp_lt_i32_e64 s[20:21], 22, v1
	v_cmp_lt_i32_e64 s[18:19], 23, v1
	v_cmp_lt_i32_e64 s[16:17], 24, v1
	v_cmp_lt_i32_e64 s[14:15], 25, v1
	v_cmp_lt_i32_e64 s[12:13], 26, v1
	v_cmp_lt_i32_e64 s[10:11], 27, v1
	v_cmp_lt_i32_e64 s[8:9], 28, v1
	v_cmp_lt_i32_e64 s[6:7], 29, v1
	v_cmp_lt_i32_e64 s[4:5], 30, v1
	v_cmp_lt_i32_e64 s[68:69], 31, v1
	s_waitcnt vmcnt(4)
	s_mov_b64 exec, s[30:31]
	v_lshlrev_b32_sdwa v46, v44, v30 dst_sel:DWORD dst_unused:UNUSED_PAD src0_sel:DWORD src1_sel:BYTE_0
	s_nop 0
	ds_add_u32 v46, v45 offset:16384
	s_mov_b64 exec, s[66:67]
	v_lshlrev_b32_sdwa v47, v44, v31 dst_sel:DWORD dst_unused:UNUSED_PAD src0_sel:DWORD src1_sel:BYTE_0
	s_nop 0
	ds_add_u32 v47, v45 offset:16384
	s_mov_b64 exec, s[64:65]
	v_lshlrev_b32_sdwa v46, v44, v32 dst_sel:DWORD dst_unused:UNUSED_PAD src0_sel:DWORD src1_sel:BYTE_0
	s_nop 0
	ds_add_u32 v46, v45 offset:16384
	s_mov_b64 exec, s[62:63]
	v_lshlrev_b32_sdwa v47, v44, v33 dst_sel:DWORD dst_unused:UNUSED_PAD src0_sel:DWORD src1_sel:BYTE_0
	s_nop 0
	ds_add_u32 v47, v45 offset:16384
	s_cmp_eq_u64 s[60:61], 0
	s_cbranch_scc1 .Lcsr_p1_done
	s_mov_b64 exec, s[60:61]
	v_lshlrev_b32_sdwa v46, v44, v26 dst_sel:DWORD dst_unused:UNUSED_PAD src0_sel:DWORD src1_sel:BYTE_0
	s_nop 0
	ds_add_u32 v46, v45 offset:16384
	s_mov_b64 exec, s[58:59]
	v_lshlrev_b32_sdwa v47, v44, v27 dst_sel:DWORD dst_unused:UNUSED_PAD src0_sel:DWORD src1_sel:BYTE_0
	s_nop 0
	ds_add_u32 v47, v45 offset:16384
	s_mov_b64 exec, s[56:57]
	v_lshlrev_b32_sdwa v46, v44, v28 dst_sel:DWORD dst_unused:UNUSED_PAD src0_sel:DWORD src1_sel:BYTE_0
	s_nop 0
	ds_add_u32 v46, v45 offset:16384
	s_mov_b64 exec, s[54:55]
	v_lshlrev_b32_sdwa v47, v44, v29 dst_sel:DWORD dst_unused:UNUSED_PAD src0_sel:DWORD src1_sel:BYTE_0
	s_nop 0
	ds_add_u32 v47, v45 offset:16384
	s_cmp_eq_u64 s[52:53], 0
	s_cbranch_scc1 .Lcsr_p1_done
	s_mov_b64 exec, s[52:53]
	v_lshlrev_b32_sdwa v46, v44, v22 dst_sel:DWORD dst_unused:UNUSED_PAD src0_sel:DWORD src1_sel:BYTE_0
	s_nop 0
	ds_add_u32 v46, v45 offset:16384
	s_mov_b64 exec, s[50:51]
	v_lshlrev_b32_sdwa v47, v44, v23 dst_sel:DWORD dst_unused:UNUSED_PAD src0_sel:DWORD src1_sel:BYTE_0
	s_nop 0
	ds_add_u32 v47, v45 offset:16384
	s_mov_b64 exec, s[48:49]
	v_lshlrev_b32_sdwa v46, v44, v24 dst_sel:DWORD dst_unused:UNUSED_PAD src0_sel:DWORD src1_sel:BYTE_0
	s_nop 0
	ds_add_u32 v46, v45 offset:16384
	s_mov_b64 exec, s[46:47]
	v_lshlrev_b32_sdwa v47, v44, v25 dst_sel:DWORD dst_unused:UNUSED_PAD src0_sel:DWORD src1_sel:BYTE_0
	s_nop 0
	ds_add_u32 v47, v45 offset:16384
	s_cmp_eq_u64 s[44:45], 0
	s_cbranch_scc1 .Lcsr_p1_done
	s_mov_b64 exec, s[44:45]
	v_lshlrev_b32_sdwa v46, v44, v18 dst_sel:DWORD dst_unused:UNUSED_PAD src0_sel:DWORD src1_sel:BYTE_0
	s_nop 0
	ds_add_u32 v46, v45 offset:16384
	s_mov_b64 exec, s[42:43]
	v_lshlrev_b32_sdwa v47, v44, v19 dst_sel:DWORD dst_unused:UNUSED_PAD src0_sel:DWORD src1_sel:BYTE_0
	s_nop 0
	ds_add_u32 v47, v45 offset:16384
	s_mov_b64 exec, s[40:41]
	v_lshlrev_b32_sdwa v46, v44, v20 dst_sel:DWORD dst_unused:UNUSED_PAD src0_sel:DWORD src1_sel:BYTE_0
	s_nop 0
	ds_add_u32 v46, v45 offset:16384
	s_mov_b64 exec, s[38:39]
	v_lshlrev_b32_sdwa v47, v44, v21 dst_sel:DWORD dst_unused:UNUSED_PAD src0_sel:DWORD src1_sel:BYTE_0
	s_nop 0
	ds_add_u32 v47, v45 offset:16384
	s_waitcnt vmcnt(0)
	s_cmp_eq_u64 s[36:37], 0
	s_cbranch_scc1 .Lcsr_p1_done
	s_mov_b64 exec, s[36:37]
	v_lshlrev_b32_sdwa v46, v44, v14 dst_sel:DWORD dst_unused:UNUSED_PAD src0_sel:DWORD src1_sel:BYTE_0
	s_nop 0
	ds_add_u32 v46, v45 offset:16384
	s_mov_b64 exec, s[34:35]
	v_lshlrev_b32_sdwa v47, v44, v15 dst_sel:DWORD dst_unused:UNUSED_PAD src0_sel:DWORD src1_sel:BYTE_0
	s_nop 0
	ds_add_u32 v47, v45 offset:16384
	s_mov_b64 exec, s[28:29]
	v_lshlrev_b32_sdwa v46, v44, v16 dst_sel:DWORD dst_unused:UNUSED_PAD src0_sel:DWORD src1_sel:BYTE_0
	s_nop 0
	ds_add_u32 v46, v45 offset:16384
	s_mov_b64 exec, s[26:27]
	v_lshlrev_b32_sdwa v47, v44, v17 dst_sel:DWORD dst_unused:UNUSED_PAD src0_sel:DWORD src1_sel:BYTE_0
	s_nop 0
	ds_add_u32 v47, v45 offset:16384
	s_cmp_eq_u64 s[24:25], 0
	s_cbranch_scc1 .Lcsr_p1_done
	s_mov_b64 exec, s[24:25]
	v_lshlrev_b32_sdwa v46, v44, v10 dst_sel:DWORD dst_unused:UNUSED_PAD src0_sel:DWORD src1_sel:BYTE_0
	s_nop 0
	ds_add_u32 v46, v45 offset:16384
	s_mov_b64 exec, s[22:23]
	v_lshlrev_b32_sdwa v47, v44, v11 dst_sel:DWORD dst_unused:UNUSED_PAD src0_sel:DWORD src1_sel:BYTE_0
	s_nop 0
	ds_add_u32 v47, v45 offset:16384
	s_mov_b64 exec, s[20:21]
	v_lshlrev_b32_sdwa v46, v44, v12 dst_sel:DWORD dst_unused:UNUSED_PAD src0_sel:DWORD src1_sel:BYTE_0
	s_nop 0
	ds_add_u32 v46, v45 offset:16384
	s_mov_b64 exec, s[18:19]
	v_lshlrev_b32_sdwa v47, v44, v13 dst_sel:DWORD dst_unused:UNUSED_PAD src0_sel:DWORD src1_sel:BYTE_0
	s_nop 0
	ds_add_u32 v47, v45 offset:16384
	s_cmp_eq_u64 s[16:17], 0
	s_cbranch_scc1 .Lcsr_p1_done
	s_mov_b64 exec, s[16:17]
	v_lshlrev_b32_sdwa v46, v44, v6 dst_sel:DWORD dst_unused:UNUSED_PAD src0_sel:DWORD src1_sel:BYTE_0
	s_nop 0
	ds_add_u32 v46, v45 offset:16384
	s_mov_b64 exec, s[14:15]
	v_lshlrev_b32_sdwa v47, v44, v7 dst_sel:DWORD dst_unused:UNUSED_PAD src0_sel:DWORD src1_sel:BYTE_0
	s_nop 0
	ds_add_u32 v47, v45 offset:16384
	s_mov_b64 exec, s[12:13]
	v_lshlrev_b32_sdwa v46, v44, v8 dst_sel:DWORD dst_unused:UNUSED_PAD src0_sel:DWORD src1_sel:BYTE_0
	s_nop 0
	ds_add_u32 v46, v45 offset:16384
	s_mov_b64 exec, s[10:11]
	v_lshlrev_b32_sdwa v47, v44, v9 dst_sel:DWORD dst_unused:UNUSED_PAD src0_sel:DWORD src1_sel:BYTE_0
	s_nop 0
	ds_add_u32 v47, v45 offset:16384
	s_cmp_eq_u64 s[8:9], 0
	s_cbranch_scc1 .Lcsr_p1_done
	s_mov_b64 exec, s[8:9]
	v_lshlrev_b32_sdwa v46, v44, v2 dst_sel:DWORD dst_unused:UNUSED_PAD src0_sel:DWORD src1_sel:BYTE_0
	s_nop 0
	ds_add_u32 v46, v45 offset:16384
	s_mov_b64 exec, s[6:7]
	v_lshlrev_b32_sdwa v47, v44, v3 dst_sel:DWORD dst_unused:UNUSED_PAD src0_sel:DWORD src1_sel:BYTE_0
	s_nop 0
	ds_add_u32 v47, v45 offset:16384
	s_mov_b64 exec, s[4:5]
	v_lshlrev_b32_sdwa v46, v44, v4 dst_sel:DWORD dst_unused:UNUSED_PAD src0_sel:DWORD src1_sel:BYTE_0
	s_nop 0
	ds_add_u32 v46, v45 offset:16384
	s_mov_b64 exec, s[68:69]
	v_lshlrev_b32_sdwa v47, v44, v5 dst_sel:DWORD dst_unused:UNUSED_PAD src0_sel:DWORD src1_sel:BYTE_0
	s_nop 0
	ds_add_u32 v47, v45 offset:16384
.Lcsr_p1_done:
	s_mov_b64 exec, s[0:1]
	s_mov_b32 s3, 32
	v_cmp_lt_i32_e64 s[0:1], 32, v1
	v_lshl_add_u64 v[34:35], v[34:35], 2, v[38:39]
	s_and_saveexec_b64 s[80:81], s[0:1]
	s_cbranch_execz .LBB1_43
	v_lshl_add_u64 v[38:39], s[84:85], 0, v[34:35]
	s_mov_b64 s[70:71], 0x80
	v_lshl_add_u64 v[38:39], v[38:39], 0, s[70:71]
	s_mov_b64 s[82:83], 0
	v_mov_b32_e32 v44, 1
	v_mov_b32_e32 v45, 2
